# baseline (speedup 1.0000x reference)
.LBB2_382:
	ds_read_b128 v[152:155], v151
	ds_read_b128 v[156:159], v151 offset:1024
	ds_read_b128 v[164:167], v151 offset:2048
	ds_read_b128 v[168:171], v151 offset:3072
	s_lshl_b32 s58, s84, 7
	s_add_u32 s59, s24, s58
	s_addc_u32 s91, s25, 0
	s_add_u32 s92, s59, 0x80
	s_addc_u32 s93, s91, 0
	s_add_i32 s56, s52, 0xc000
	s_mov_b32 m0, s56
	s_add_i32 s33, s52, 0xe000
	ds_read_b128 v[172:175], v147
	ds_read_b128 v[176:179], v147 offset:1024
	ds_read_b128 v[184:187], v146
	ds_read_b128 v[188:191], v146 offset:1024
	ds_read_b128 v[192:195], v145
	ds_read_b128 v[196:199], v145 offset:1024
	ds_read_b128 v[200:203], v144
	ds_read_b128 v[204:207], v144 offset:1024
	global_load_lds_dwordx4 v132, s[92:93]
	s_mov_b32 m0, s33
	s_nop 0
	global_load_lds_dwordx4 v130, s[92:93]
	s_waitcnt lgkmcnt(8)
	s_barrier
	s_waitcnt lgkmcnt(0)
	v_mfma_f32_16x16x32_f16 v[126:129], v[152:155], v[172:175], v[126:129]
	v_mfma_f32_16x16x32_f16 v[122:125], v[164:167], v[172:175], v[122:125]
	ds_read_b128 v[208:211], v150
	v_mfma_f32_16x16x32_f16 v[118:121], v[152:155], v[184:187], v[118:121]
	v_mfma_f32_16x16x32_f16 v[114:117], v[164:167], v[184:187], v[114:117]
	ds_read_b128 v[212:215], v150 offset:1024
	v_mfma_f32_16x16x32_f16 v[110:113], v[152:155], v[192:195], v[110:113]
	v_mfma_f32_16x16x32_f16 v[106:109], v[164:167], v[192:195], v[106:109]
	ds_read_b128 v[216:219], v150 offset:2048
	v_mfma_f32_16x16x32_f16 v[102:105], v[152:155], v[200:203], v[102:105]
	v_mfma_f32_16x16x32_f16 v[98:101], v[164:167], v[200:203], v[98:101]
	ds_read_b128 v[220:223], v150 offset:3072
	v_mfma_f32_16x16x32_f16 v[126:129], v[156:159], v[176:179], v[126:129]
	v_mfma_f32_16x16x32_f16 v[122:125], v[168:171], v[176:179], v[122:125]
	v_mfma_f32_16x16x32_f16 v[118:121], v[156:159], v[188:191], v[118:121]
	v_mfma_f32_16x16x32_f16 v[114:117], v[168:171], v[188:191], v[114:117]
	v_mfma_f32_16x16x32_f16 v[110:113], v[156:159], v[196:199], v[110:113]
	v_mfma_f32_16x16x32_f16 v[106:109], v[168:171], v[196:199], v[106:109]
	v_mfma_f32_16x16x32_f16 v[102:105], v[156:159], v[204:207], v[102:105]
	v_mfma_f32_16x16x32_f16 v[98:101], v[168:171], v[204:207], v[98:101]
	s_barrier
	s_add_i32 s57, s84, 2
	s_lshl_b32 s82, s57, 7
	s_add_u32 s92, s4, s82
	s_addc_u32 s93, s5, 0
	s_mov_b32 m0, s53
	global_load_lds_dwordx4 v162, s[92:93]
	s_mov_b32 m0, s55
	s_add_u32 s92, s92, 0x40000
	s_addc_u32 s93, s93, 0
	global_load_lds_dwordx4 v162, s[92:93]
	s_barrier
	s_waitcnt lgkmcnt(0)
	v_mfma_f32_16x16x32_f16 v[94:97], v[208:211], v[172:175], v[94:97]
	v_mfma_f32_16x16x32_f16 v[90:93], v[216:219], v[172:175], v[90:93]
	v_mfma_f32_16x16x32_f16 v[86:89], v[208:211], v[184:187], v[86:89]
	v_mfma_f32_16x16x32_f16 v[82:85], v[216:219], v[184:187], v[82:85]
	v_mfma_f32_16x16x32_f16 v[78:81], v[208:211], v[192:195], v[78:81]
	v_mfma_f32_16x16x32_f16 v[74:77], v[216:219], v[192:195], v[74:77]
	v_mfma_f32_16x16x32_f16 v[70:73], v[208:211], v[200:203], v[70:73]
	v_mfma_f32_16x16x32_f16 v[66:69], v[216:219], v[200:203], v[66:69]
	v_mfma_f32_16x16x32_f16 v[94:97], v[212:215], v[176:179], v[94:97]
	v_mfma_f32_16x16x32_f16 v[90:93], v[220:223], v[176:179], v[90:93]
	v_mfma_f32_16x16x32_f16 v[86:89], v[212:215], v[188:191], v[86:89]
	v_mfma_f32_16x16x32_f16 v[82:85], v[220:223], v[188:191], v[82:85]
	v_mfma_f32_16x16x32_f16 v[78:81], v[212:215], v[196:199], v[78:81]
	v_mfma_f32_16x16x32_f16 v[74:77], v[220:223], v[196:199], v[74:77]
	v_mfma_f32_16x16x32_f16 v[70:73], v[212:215], v[204:207], v[70:73]
	v_mfma_f32_16x16x32_f16 v[66:69], v[220:223], v[204:207], v[66:69]
	s_add_u32 s92, s24, s82
	s_addc_u32 s93, s25, 0
	s_mov_b32 m0, s52
	s_barrier
	ds_read_b128 v[172:175], v147 offset:16384
	ds_read_b128 v[176:179], v147 offset:17408
	ds_read_b128 v[184:187], v146 offset:16384
	ds_read_b128 v[188:191], v146 offset:17408
	ds_read_b128 v[192:195], v145 offset:16384
	ds_read_b128 v[196:199], v145 offset:17408
	ds_read_b128 v[200:203], v144 offset:16384
	ds_read_b128 v[204:207], v144 offset:17408
	global_load_lds_dwordx4 v134, s[92:93]
	s_mov_b32 m0, s86
	s_nop 0
	global_load_lds_dwordx4 v136, s[92:93]
	s_barrier
	s_waitcnt lgkmcnt(0)
	v_mfma_f32_16x16x32_f16 v[62:65], v[152:155], v[172:175], v[62:65]
	v_mfma_f32_16x16x32_f16 v[58:61], v[164:167], v[172:175], v[58:61]
	v_mfma_f32_16x16x32_f16 v[54:57], v[152:155], v[184:187], v[54:57]
	v_mfma_f32_16x16x32_f16 v[50:53], v[164:167], v[184:187], v[50:53]
	v_mfma_f32_16x16x32_f16 v[46:49], v[152:155], v[192:195], v[46:49]
	v_mfma_f32_16x16x32_f16 v[42:45], v[164:167], v[192:195], v[42:45]
	v_mfma_f32_16x16x32_f16 v[38:41], v[152:155], v[200:203], v[38:41]
	v_mfma_f32_16x16x32_f16 v[34:37], v[164:167], v[200:203], v[34:37]
	v_mfma_f32_16x16x32_f16 v[62:65], v[156:159], v[176:179], v[62:65]
	v_mfma_f32_16x16x32_f16 v[58:61], v[168:171], v[176:179], v[58:61]
	v_mfma_f32_16x16x32_f16 v[54:57], v[156:159], v[188:191], v[54:57]
	v_mfma_f32_16x16x32_f16 v[50:53], v[168:171], v[188:191], v[50:53]
	v_mfma_f32_16x16x32_f16 v[46:49], v[156:159], v[196:199], v[46:49]
	v_mfma_f32_16x16x32_f16 v[42:45], v[168:171], v[196:199], v[42:45]
	v_mfma_f32_16x16x32_f16 v[38:41], v[156:159], v[204:207], v[38:41]
	v_mfma_f32_16x16x32_f16 v[34:37], v[168:171], v[204:207], v[34:37]
	s_barrier
	s_add_u32 s94, s10, s82
	s_addc_u32 s95, s11, 0
	s_mov_b32 m0, s87
	s_nop 0
	global_load_lds_dwordx4 v162, s[94:95]
	s_mov_b32 m0, s88
	s_add_u32 s94, s94, 0x40000
	s_addc_u32 s95, s95, 0
	global_load_lds_dwordx4 v162, s[94:95]
	s_waitcnt vmcnt(6)
	s_barrier
	v_mfma_f32_16x16x32_f16 v[30:33], v[208:211], v[172:175], v[30:33]
	v_mfma_f32_16x16x32_f16 v[26:29], v[216:219], v[172:175], v[26:29]
	v_mfma_f32_16x16x32_f16 v[22:25], v[208:211], v[184:187], v[22:25]
	v_mfma_f32_16x16x32_f16 v[18:21], v[216:219], v[184:187], v[18:21]
	v_mfma_f32_16x16x32_f16 v[14:17], v[208:211], v[192:195], v[14:17]
	v_mfma_f32_16x16x32_f16 v[10:13], v[216:219], v[192:195], v[10:13]
	v_mfma_f32_16x16x32_f16 v[6:9], v[208:211], v[200:203], v[6:9]
	v_mfma_f32_16x16x32_f16 v[2:5], v[216:219], v[200:203], v[2:5]
	v_mfma_f32_16x16x32_f16 v[30:33], v[212:215], v[176:179], v[30:33]
	v_mfma_f32_16x16x32_f16 v[26:29], v[220:223], v[176:179], v[26:29]
	v_mfma_f32_16x16x32_f16 v[22:25], v[212:215], v[188:191], v[22:25]
	v_mfma_f32_16x16x32_f16 v[18:21], v[220:223], v[188:191], v[18:21]
	v_mfma_f32_16x16x32_f16 v[14:17], v[212:215], v[196:199], v[14:17]
	v_mfma_f32_16x16x32_f16 v[10:13], v[220:223], v[196:199], v[10:13]
	v_mfma_f32_16x16x32_f16 v[6:9], v[212:215], v[204:207], v[6:9]
	v_mfma_f32_16x16x32_f16 v[2:5], v[220:223], v[204:207], v[2:5]
	s_barrier
	ds_read_b128 v[152:155], v149
	ds_read_b128 v[156:159], v149 offset:1024
	ds_read_b128 v[164:167], v149 offset:2048
	ds_read_b128 v[168:171], v149 offset:3072
	s_mov_b32 m0, s89
	ds_read_b128 v[172:175], v147 offset:32768
	ds_read_b128 v[176:179], v147 offset:33792
	ds_read_b128 v[184:187], v146 offset:32768
	ds_read_b128 v[188:191], v146 offset:33792
	ds_read_b128 v[192:195], v145 offset:32768
	ds_read_b128 v[196:199], v145 offset:33792
	ds_read_b128 v[200:203], v144 offset:32768
	ds_read_b128 v[204:207], v144 offset:33792
	global_load_lds_dwordx4 v132, s[92:93]
	s_mov_b32 m0, s90
	s_nop 0
	global_load_lds_dwordx4 v130, s[92:93]
	s_waitcnt lgkmcnt(8)
	s_barrier
	s_waitcnt lgkmcnt(0)
	v_mfma_f32_16x16x32_f16 v[126:129], v[152:155], v[172:175], v[126:129]
	v_mfma_f32_16x16x32_f16 v[122:125], v[164:167], v[172:175], v[122:125]
	ds_read_b128 v[208:211], v148
	v_mfma_f32_16x16x32_f16 v[118:121], v[152:155], v[184:187], v[118:121]
	v_mfma_f32_16x16x32_f16 v[114:117], v[164:167], v[184:187], v[114:117]
	ds_read_b128 v[212:215], v148 offset:1024
	v_mfma_f32_16x16x32_f16 v[110:113], v[152:155], v[192:195], v[110:113]
	v_mfma_f32_16x16x32_f16 v[106:109], v[164:167], v[192:195], v[106:109]
	ds_read_b128 v[216:219], v148 offset:2048
	v_mfma_f32_16x16x32_f16 v[102:105], v[152:155], v[200:203], v[102:105]
	v_mfma_f32_16x16x32_f16 v[98:101], v[164:167], v[200:203], v[98:101]
	ds_read_b128 v[220:223], v148 offset:3072
	v_mfma_f32_16x16x32_f16 v[126:129], v[156:159], v[176:179], v[126:129]
	v_mfma_f32_16x16x32_f16 v[122:125], v[168:171], v[176:179], v[122:125]
	v_mfma_f32_16x16x32_f16 v[118:121], v[156:159], v[188:191], v[118:121]
	v_mfma_f32_16x16x32_f16 v[114:117], v[168:171], v[188:191], v[114:117]
	v_mfma_f32_16x16x32_f16 v[110:113], v[156:159], v[196:199], v[110:113]
	v_mfma_f32_16x16x32_f16 v[106:109], v[168:171], v[196:199], v[106:109]
	v_mfma_f32_16x16x32_f16 v[102:105], v[156:159], v[204:207], v[102:105]
	v_mfma_f32_16x16x32_f16 v[98:101], v[168:171], v[204:207], v[98:101]
	s_barrier
	s_add_u32 s82, s4, s58
	s_addc_u32 s83, s5, 0
	s_add_u32 s92, s82, 0x180
	s_addc_u32 s93, s83, 0
	s_add_i32 m0, s52, 0x18000
	global_load_lds_dwordx4 v162, s[92:93]
	s_add_i32 m0, s52, 0x1a000
	s_add_u32 s92, s92, 0x40000
	s_addc_u32 s93, s93, 0
	global_load_lds_dwordx4 v162, s[92:93]
	s_barrier
	s_waitcnt lgkmcnt(0)
	v_mfma_f32_16x16x32_f16 v[94:97], v[208:211], v[172:175], v[94:97]
	v_mfma_f32_16x16x32_f16 v[90:93], v[216:219], v[172:175], v[90:93]
	v_mfma_f32_16x16x32_f16 v[86:89], v[208:211], v[184:187], v[86:89]
	v_mfma_f32_16x16x32_f16 v[82:85], v[216:219], v[184:187], v[82:85]
	v_mfma_f32_16x16x32_f16 v[78:81], v[208:211], v[192:195], v[78:81]
	v_mfma_f32_16x16x32_f16 v[74:77], v[216:219], v[192:195], v[74:77]
	v_mfma_f32_16x16x32_f16 v[70:73], v[208:211], v[200:203], v[70:73]
	v_mfma_f32_16x16x32_f16 v[66:69], v[216:219], v[200:203], v[66:69]
	v_mfma_f32_16x16x32_f16 v[94:97], v[212:215], v[176:179], v[94:97]
	v_mfma_f32_16x16x32_f16 v[90:93], v[220:223], v[176:179], v[90:93]
	v_mfma_f32_16x16x32_f16 v[86:89], v[212:215], v[188:191], v[86:89]
	v_mfma_f32_16x16x32_f16 v[82:85], v[220:223], v[188:191], v[82:85]
	v_mfma_f32_16x16x32_f16 v[78:81], v[212:215], v[196:199], v[78:81]
	v_mfma_f32_16x16x32_f16 v[74:77], v[220:223], v[196:199], v[74:77]
	v_mfma_f32_16x16x32_f16 v[70:73], v[212:215], v[204:207], v[70:73]
	v_mfma_f32_16x16x32_f16 v[66:69], v[220:223], v[204:207], v[66:69]
	s_add_u32 s92, s59, 0x180
	s_addc_u32 s93, s91, 0
	s_mov_b32 m0, s34
	s_barrier
	ds_read_b128 v[172:175], v147 offset:49152
	ds_read_b128 v[176:179], v147 offset:50176
	ds_read_b128 v[184:187], v146 offset:49152
	ds_read_b128 v[188:191], v146 offset:50176
	ds_read_b128 v[192:195], v145 offset:49152
	ds_read_b128 v[196:199], v145 offset:50176
	ds_read_b128 v[200:203], v144 offset:49152
	ds_read_b128 v[204:207], v144 offset:50176
	global_load_lds_dwordx4 v134, s[92:93]
	s_mov_b32 m0, s35
	s_nop 0
	global_load_lds_dwordx4 v136, s[92:93]
	s_barrier
	s_waitcnt lgkmcnt(0)
	v_mfma_f32_16x16x32_f16 v[62:65], v[152:155], v[172:175], v[62:65]
	v_mfma_f32_16x16x32_f16 v[58:61], v[164:167], v[172:175], v[58:61]
	v_mfma_f32_16x16x32_f16 v[54:57], v[152:155], v[184:187], v[54:57]
	v_mfma_f32_16x16x32_f16 v[50:53], v[164:167], v[184:187], v[50:53]
	v_mfma_f32_16x16x32_f16 v[46:49], v[152:155], v[192:195], v[46:49]
	v_mfma_f32_16x16x32_f16 v[42:45], v[164:167], v[192:195], v[42:45]
	v_mfma_f32_16x16x32_f16 v[38:41], v[152:155], v[200:203], v[38:41]
	v_mfma_f32_16x16x32_f16 v[34:37], v[164:167], v[200:203], v[34:37]
	v_mfma_f32_16x16x32_f16 v[62:65], v[156:159], v[176:179], v[62:65]
	v_mfma_f32_16x16x32_f16 v[58:61], v[168:171], v[176:179], v[58:61]
	v_mfma_f32_16x16x32_f16 v[54:57], v[156:159], v[188:191], v[54:57]
	v_mfma_f32_16x16x32_f16 v[50:53], v[168:171], v[188:191], v[50:53]
	v_mfma_f32_16x16x32_f16 v[46:49], v[156:159], v[196:199], v[46:49]
	v_mfma_f32_16x16x32_f16 v[42:45], v[168:171], v[196:199], v[42:45]
	v_mfma_f32_16x16x32_f16 v[38:41], v[156:159], v[204:207], v[38:41]
	v_mfma_f32_16x16x32_f16 v[34:37], v[168:171], v[204:207], v[34:37]
	s_barrier
	s_add_u32 s58, s10, s58
	s_addc_u32 s59, s11, 0
	s_add_u32 s58, s58, 0x180
	s_addc_u32 s59, s59, 0
	s_add_i32 m0, s52, 0x1c000
	s_nop 0
	global_load_lds_dwordx4 v162, s[58:59]
	s_add_i32 m0, s52, 0x1e000
	s_add_u32 s58, s58, 0x40000
	s_addc_u32 s59, s59, 0
	global_load_lds_dwordx4 v162, s[58:59]
	s_waitcnt vmcnt(6)
	s_barrier
	v_mfma_f32_16x16x32_f16 v[30:33], v[208:211], v[172:175], v[30:33]
	v_mfma_f32_16x16x32_f16 v[26:29], v[216:219], v[172:175], v[26:29]
	v_mfma_f32_16x16x32_f16 v[22:25], v[208:211], v[184:187], v[22:25]
	v_mfma_f32_16x16x32_f16 v[18:21], v[216:219], v[184:187], v[18:21]
	v_mfma_f32_16x16x32_f16 v[14:17], v[208:211], v[192:195], v[14:17]
	v_mfma_f32_16x16x32_f16 v[10:13], v[216:219], v[192:195], v[10:13]
	v_mfma_f32_16x16x32_f16 v[6:9], v[208:211], v[200:203], v[6:9]
	v_mfma_f32_16x16x32_f16 v[2:5], v[216:219], v[200:203], v[2:5]
	v_mfma_f32_16x16x32_f16 v[30:33], v[212:215], v[176:179], v[30:33]
	v_mfma_f32_16x16x32_f16 v[26:29], v[220:223], v[176:179], v[26:29]
	v_mfma_f32_16x16x32_f16 v[22:25], v[212:215], v[188:191], v[22:25]
	v_mfma_f32_16x16x32_f16 v[18:21], v[220:223], v[188:191], v[18:21]
	v_mfma_f32_16x16x32_f16 v[14:17], v[212:215], v[196:199], v[14:17]
	v_mfma_f32_16x16x32_f16 v[10:13], v[220:223], v[196:199], v[10:13]
	v_mfma_f32_16x16x32_f16 v[6:9], v[212:215], v[204:207], v[6:9]
	v_mfma_f32_16x16x32_f16 v[2:5], v[220:223], v[204:207], v[2:5]
	s_cmp_lt_u32 s84, 28
	s_mov_b32 s84, s57
	s_barrier
	s_cbranch_scc1 .LBB2_382
	v_readlane_b32 s4, v244, 8
	v_readlane_b32 s5, v244, 9
	s_mov_b32 m0, s56
	ds_read_b128 v[134:137], v151
	ds_read_b128 v[152:155], v151 offset:1024
	ds_read_b128 v[156:159], v151 offset:2048
	ds_read_b128 v[164:167], v151 offset:3072
	ds_read_b128 v[168:171], v147
	ds_read_b128 v[172:175], v147 offset:1024
	ds_read_b128 v[176:179], v146
	ds_read_b128 v[184:187], v146 offset:1024
	ds_read_b128 v[188:191], v145
	ds_read_b128 v[192:195], v145 offset:1024
	ds_read_b128 v[196:199], v144
	ds_read_b128 v[200:203], v144 offset:1024
	v_lshl_add_u64 v[132:133], s[4:5], 0, v[132:133]
	global_load_lds_dwordx4 v[132:133], off
	v_lshl_add_u64 v[130:131], s[4:5], 0, v[130:131]
	s_mov_b32 m0, s33
	s_nop 0
	global_load_lds_dwordx4 v[130:131], off
	s_barrier
	s_waitcnt lgkmcnt(0)
	v_mfma_f32_16x16x32_f16 v[126:129], v[134:137], v[168:171], v[126:129]
	v_mfma_f32_16x16x32_f16 v[122:125], v[156:159], v[168:171], v[122:125]
	v_mfma_f32_16x16x32_f16 v[110:113], v[134:137], v[188:191], v[110:113]
	v_mfma_f32_16x16x32_f16 v[106:109], v[156:159], v[188:191], v[106:109]
	v_mfma_f32_16x16x32_f16 v[126:129], v[152:155], v[172:175], v[126:129]
	v_mfma_f32_16x16x32_f16 v[122:125], v[164:167], v[172:175], v[122:125]
	v_mfma_f32_16x16x32_f16 v[118:121], v[134:137], v[176:179], v[118:121]
	v_mfma_f32_16x16x32_f16 v[114:117], v[156:159], v[176:179], v[114:117]
	v_mfma_f32_16x16x32_f16 v[110:113], v[152:155], v[192:195], v[110:113]
	v_mfma_f32_16x16x32_f16 v[106:109], v[164:167], v[192:195], v[106:109]
	v_mfma_f32_16x16x32_f16 v[102:105], v[134:137], v[196:199], v[102:105]
	v_mfma_f32_16x16x32_f16 v[98:101], v[156:159], v[196:199], v[98:101]
	v_mfma_f32_16x16x32_f16 v[130:133], v[152:155], v[184:187], v[118:121]
	v_mfma_f32_16x16x32_f16 v[204:207], v[164:167], v[184:187], v[114:117]
	v_mfma_f32_16x16x32_f16 v[208:211], v[152:155], v[200:203], v[102:105]
	v_mfma_f32_16x16x32_f16 v[212:215], v[164:167], v[200:203], v[98:101]
	s_barrier
	s_nop 1
	ds_read_b128 v[98:101], v150
	ds_read_b128 v[102:105], v150 offset:1024
	ds_read_b128 v[114:117], v150 offset:2048
	ds_read_b128 v[118:121], v150 offset:3072
	s_barrier
	s_waitcnt lgkmcnt(0)
	v_mfma_f32_16x16x32_f16 v[94:97], v[98:101], v[168:171], v[94:97]
	v_mfma_f32_16x16x32_f16 v[90:93], v[114:117], v[168:171], v[90:93]
	v_mfma_f32_16x16x32_f16 v[78:81], v[98:101], v[188:191], v[78:81]
	v_mfma_f32_16x16x32_f16 v[74:77], v[114:117], v[188:191], v[74:77]
	v_mfma_f32_16x16x32_f16 v[94:97], v[102:105], v[172:175], v[94:97]
	v_mfma_f32_16x16x32_f16 v[90:93], v[118:121], v[172:175], v[90:93]
	v_mfma_f32_16x16x32_f16 v[86:89], v[98:101], v[176:179], v[86:89]
	v_mfma_f32_16x16x32_f16 v[82:85], v[114:117], v[176:179], v[82:85]
	v_mfma_f32_16x16x32_f16 v[78:81], v[102:105], v[192:195], v[78:81]
	v_mfma_f32_16x16x32_f16 v[74:77], v[118:121], v[192:195], v[74:77]
	v_mfma_f32_16x16x32_f16 v[70:73], v[98:101], v[196:199], v[70:73]
	v_mfma_f32_16x16x32_f16 v[66:69], v[114:117], v[196:199], v[66:69]
	v_mfma_f32_16x16x32_f16 v[168:171], v[102:105], v[184:187], v[86:89]
	v_mfma_f32_16x16x32_f16 v[172:175], v[118:121], v[184:187], v[82:85]
	v_mfma_f32_16x16x32_f16 v[176:179], v[102:105], v[200:203], v[70:73]
	v_mfma_f32_16x16x32_f16 v[184:187], v[118:121], v[200:203], v[66:69]
	s_barrier
	s_nop 1
	ds_read_b128 v[66:69], v147 offset:16384
	ds_read_b128 v[70:73], v147 offset:17408
	ds_read_b128 v[82:85], v146 offset:16384
	ds_read_b128 v[86:89], v146 offset:17408
	ds_read_b128 v[188:191], v145 offset:16384
	ds_read_b128 v[192:195], v145 offset:17408
	ds_read_b128 v[196:199], v144 offset:16384
	ds_read_b128 v[200:203], v144 offset:17408
	s_waitcnt vmcnt(4)
	s_barrier
	s_waitcnt lgkmcnt(0)
	v_mfma_f32_16x16x32_f16 v[62:65], v[134:137], v[66:69], v[62:65]
	v_mfma_f32_16x16x32_f16 v[58:61], v[156:159], v[66:69], v[58:61]
	v_mfma_f32_16x16x32_f16 v[46:49], v[134:137], v[188:191], v[46:49]
	v_mfma_f32_16x16x32_f16 v[42:45], v[156:159], v[188:191], v[42:45]
	v_mfma_f32_16x16x32_f16 v[62:65], v[152:155], v[70:73], v[62:65]
	v_mfma_f32_16x16x32_f16 v[58:61], v[164:167], v[70:73], v[58:61]
	v_mfma_f32_16x16x32_f16 v[54:57], v[134:137], v[82:85], v[54:57]
	v_mfma_f32_16x16x32_f16 v[50:53], v[156:159], v[82:85], v[50:53]
	v_mfma_f32_16x16x32_f16 v[46:49], v[152:155], v[192:195], v[46:49]
	v_mfma_f32_16x16x32_f16 v[42:45], v[164:167], v[192:195], v[42:45]
	v_mfma_f32_16x16x32_f16 v[38:41], v[134:137], v[196:199], v[38:41]
	v_mfma_f32_16x16x32_f16 v[34:37], v[156:159], v[196:199], v[34:37]
	v_mfma_f32_16x16x32_f16 v[216:219], v[152:155], v[86:89], v[54:57]
	v_mfma_f32_16x16x32_f16 v[220:223], v[164:167], v[86:89], v[50:53]
	v_mfma_f32_16x16x32_f16 v[134:137], v[152:155], v[200:203], v[38:41]
	v_mfma_f32_16x16x32_f16 v[150:153], v[164:167], v[200:203], v[34:37]
	v_mfma_f32_16x16x32_f16 v[30:33], v[98:101], v[66:69], v[30:33]
	v_mfma_f32_16x16x32_f16 v[26:29], v[114:117], v[66:69], v[26:29]
	v_mfma_f32_16x16x32_f16 v[14:17], v[98:101], v[188:191], v[14:17]
	v_mfma_f32_16x16x32_f16 v[10:13], v[114:117], v[188:191], v[10:13]
	v_mfma_f32_16x16x32_f16 v[30:33], v[102:105], v[70:73], v[30:33]
	v_mfma_f32_16x16x32_f16 v[26:29], v[118:121], v[70:73], v[26:29]
	v_mfma_f32_16x16x32_f16 v[22:25], v[98:101], v[82:85], v[22:25]
	v_mfma_f32_16x16x32_f16 v[18:21], v[114:117], v[82:85], v[18:21]
	v_mfma_f32_16x16x32_f16 v[14:17], v[102:105], v[192:195], v[14:17]
	v_mfma_f32_16x16x32_f16 v[10:13], v[118:121], v[192:195], v[10:13]
	v_mfma_f32_16x16x32_f16 v[6:9], v[98:101], v[196:199], v[6:9]
	v_mfma_f32_16x16x32_f16 v[2:5], v[114:117], v[196:199], v[2:5]
	v_mfma_f32_16x16x32_f16 v[154:157], v[102:105], v[86:89], v[22:25]
	v_mfma_f32_16x16x32_f16 v[158:161], v[118:121], v[86:89], v[18:21]
	v_mfma_f32_16x16x32_f16 v[164:167], v[102:105], v[200:203], v[6:9]
	v_mfma_f32_16x16x32_f16 v[188:191], v[118:121], v[200:203], v[2:5]
	s_barrier
	s_nop 1
	ds_read_b128 v[2:5], v149
	ds_read_b128 v[6:9], v149 offset:1024
	ds_read_b128 v[192:195], v149 offset:2048
	ds_read_b128 v[196:199], v149 offset:3072
	ds_read_b128 v[18:21], v147 offset:32768
	ds_read_b128 v[22:25], v147 offset:33792
	ds_read_b128 v[34:37], v146 offset:32768
	ds_read_b128 v[38:41], v146 offset:33792
	ds_read_b128 v[50:53], v145 offset:32768
	ds_read_b128 v[54:57], v145 offset:33792
	ds_read_b128 v[200:203], v144 offset:32768
	ds_read_b128 v[224:227], v144 offset:33792
	s_waitcnt vmcnt(2)
	s_barrier
	s_waitcnt lgkmcnt(0)
	v_mfma_f32_16x16x32_f16 v[66:69], v[2:5], v[18:21], v[126:129]
	v_mfma_f32_16x16x32_f16 v[118:121], v[6:9], v[22:25], v[66:69]
	v_mfma_f32_16x16x32_f16 v[66:69], v[192:195], v[18:21], v[122:125]
	v_mfma_f32_16x16x32_f16 v[114:117], v[196:199], v[22:25], v[66:69]
	v_mfma_f32_16x16x32_f16 v[66:69], v[2:5], v[34:37], v[130:133]
	v_mfma_f32_16x16x32_f16 v[102:105], v[6:9], v[38:41], v[66:69]
	v_mfma_f32_16x16x32_f16 v[66:69], v[192:195], v[34:37], v[204:207]
	v_mfma_f32_16x16x32_f16 v[98:101], v[196:199], v[38:41], v[66:69]
	v_mfma_f32_16x16x32_f16 v[66:69], v[2:5], v[50:53], v[110:113]
	v_mfma_f32_16x16x32_f16 v[86:89], v[6:9], v[54:57], v[66:69]
	v_mfma_f32_16x16x32_f16 v[66:69], v[192:195], v[50:53], v[106:109]
	v_mfma_f32_16x16x32_f16 v[82:85], v[196:199], v[54:57], v[66:69]
	v_mfma_f32_16x16x32_f16 v[66:69], v[2:5], v[200:203], v[208:211]
	v_mfma_f32_16x16x32_f16 v[70:73], v[6:9], v[224:227], v[66:69]
	v_mfma_f32_16x16x32_f16 v[66:69], v[192:195], v[200:203], v[212:215]
	v_mfma_f32_16x16x32_f16 v[66:69], v[196:199], v[224:227], v[66:69]
	s_barrier
	ds_read_b128 v[130:133], v148
	ds_read_b128 v[204:207], v148 offset:1024
	ds_read_b128 v[208:211], v148 offset:2048
	ds_read_b128 v[212:215], v148 offset:3072
	s_waitcnt vmcnt(0)
	s_barrier
	s_waitcnt lgkmcnt(0)
	v_mfma_f32_16x16x32_f16 v[94:97], v[130:133], v[18:21], v[94:97]
	v_mfma_f32_16x16x32_f16 v[18:21], v[208:211], v[18:21], v[90:93]
	v_mfma_f32_16x16x32_f16 v[122:125], v[212:215], v[22:25], v[18:21]
	v_mfma_f32_16x16x32_f16 v[18:21], v[130:133], v[34:37], v[168:171]
	v_mfma_f32_16x16x32_f16 v[110:113], v[204:207], v[38:41], v[18:21]
	v_mfma_f32_16x16x32_f16 v[18:21], v[208:211], v[34:37], v[172:175]
	v_mfma_f32_16x16x32_f16 v[106:109], v[212:215], v[38:41], v[18:21]
	v_mfma_f32_16x16x32_f16 v[18:21], v[130:133], v[50:53], v[78:81]
	v_mfma_f32_16x16x32_f16 v[126:129], v[204:207], v[22:25], v[94:97]
	v_mfma_f32_16x16x32_f16 v[94:97], v[204:207], v[54:57], v[18:21]
	v_mfma_f32_16x16x32_f16 v[18:21], v[208:211], v[50:53], v[74:77]
	v_mfma_f32_16x16x32_f16 v[90:93], v[212:215], v[54:57], v[18:21]
	v_mfma_f32_16x16x32_f16 v[18:21], v[130:133], v[200:203], v[176:179]
	v_mfma_f32_16x16x32_f16 v[78:81], v[204:207], v[224:227], v[18:21]
	v_mfma_f32_16x16x32_f16 v[18:21], v[208:211], v[200:203], v[184:187]
	v_mfma_f32_16x16x32_f16 v[74:77], v[212:215], v[224:227], v[18:21]
	s_barrier
	ds_read_b128 v[168:171], v147 offset:49152
	ds_read_b128 v[172:175], v147 offset:50176
	ds_read_b128 v[176:179], v146 offset:49152
	ds_read_b128 v[146:149], v146 offset:50176
	ds_read_b128 v[184:187], v145 offset:49152
	ds_read_b128 v[200:203], v145 offset:50176
	ds_read_b128 v[224:227], v144 offset:49152
	ds_read_b128 v[228:231], v144 offset:50176
	s_barrier
	s_waitcnt lgkmcnt(0)
	v_mfma_f32_16x16x32_f16 v[18:21], v[2:5], v[168:171], v[62:65]
	v_mfma_f32_16x16x32_f16 v[54:57], v[6:9], v[172:175], v[18:21]
	v_mfma_f32_16x16x32_f16 v[18:21], v[192:195], v[168:171], v[58:61]
	v_mfma_f32_16x16x32_f16 v[50:53], v[196:199], v[172:175], v[18:21]
	v_mfma_f32_16x16x32_f16 v[18:21], v[2:5], v[176:179], v[216:219]
	v_mfma_f32_16x16x32_f16 v[38:41], v[6:9], v[146:149], v[18:21]
	v_mfma_f32_16x16x32_f16 v[18:21], v[192:195], v[176:179], v[220:223]
	v_mfma_f32_16x16x32_f16 v[34:37], v[196:199], v[146:149], v[18:21]
	v_mfma_f32_16x16x32_f16 v[18:21], v[2:5], v[184:187], v[46:49]
	v_mfma_f32_16x16x32_f16 v[2:5], v[2:5], v[224:227], v[134:137]
	v_mfma_f32_16x16x32_f16 v[22:25], v[6:9], v[200:203], v[18:21]
	v_mfma_f32_16x16x32_f16 v[18:21], v[192:195], v[184:187], v[42:45]
	v_mfma_f32_16x16x32_f16 v[6:9], v[6:9], v[228:231], v[2:5]
	v_mfma_f32_16x16x32_f16 v[2:5], v[192:195], v[224:227], v[150:153]
	v_mfma_f32_16x16x32_f16 v[18:21], v[196:199], v[200:203], v[18:21]
	v_mfma_f32_16x16x32_f16 v[2:5], v[196:199], v[228:231], v[2:5]
	v_mfma_f32_16x16x32_f16 v[26:29], v[208:211], v[168:171], v[26:29]
	v_mfma_f32_16x16x32_f16 v[58:61], v[212:215], v[172:175], v[26:29]
	v_mfma_f32_16x16x32_f16 v[26:29], v[130:133], v[176:179], v[154:157]
	v_mfma_f32_16x16x32_f16 v[46:49], v[204:207], v[146:149], v[26:29]
	v_mfma_f32_16x16x32_f16 v[26:29], v[208:211], v[176:179], v[158:161]
	v_mfma_f32_16x16x32_f16 v[10:13], v[208:211], v[184:187], v[10:13]
	v_mfma_f32_16x16x32_f16 v[30:33], v[130:133], v[168:171], v[30:33]
	v_mfma_f32_16x16x32_f16 v[42:45], v[212:215], v[146:149], v[26:29]
	v_mfma_f32_16x16x32_f16 v[14:17], v[130:133], v[184:187], v[14:17]
	v_mfma_f32_16x16x32_f16 v[26:29], v[212:215], v[200:203], v[10:13]
	v_mfma_f32_16x16x32_f16 v[10:13], v[130:133], v[224:227], v[164:167]
	v_mfma_f32_16x16x32_f16 v[62:65], v[204:207], v[172:175], v[30:33]
	v_mfma_f32_16x16x32_f16 v[30:33], v[204:207], v[200:203], v[14:17]
	v_mfma_f32_16x16x32_f16 v[14:17], v[204:207], v[228:231], v[10:13]
	v_mfma_f32_16x16x32_f16 v[10:13], v[208:211], v[224:227], v[188:191]
	v_mfma_f32_16x16x32_f16 v[10:13], v[212:215], v[228:231], v[10:13]
